# baseline (speedup 1.0000x reference)
.Lk2f_l3:
	s_waitcnt vmcnt(0)
	s_cmp_lt_u32 s4, 4
	s_cbranch_scc0 .Lk2f_l4
	v_sub_u32_e32 v24, v9, v8
	v_min_u32_e32 v25, 0xf4, v0
	v_lshlrev_b32_e32 v25, 14, v25
	v_lshl_add_u32 v25, v8, 2, v25
	global_load_dwordx4 v[26:29], v25, s[10:11]
	global_load_dwordx4 v[30:33], v25, s[10:11] offset:16
	global_load_dwordx4 v[34:37], v25, s[10:11] offset:32
	global_load_dwordx4 v[38:41], v25, s[10:11] offset:48
	global_load_dwordx4 v[44:47], v25, s[10:11] offset:256
	global_load_dwordx4 v[48:51], v25, s[10:11] offset:384
	global_load_dwordx4 v[52:55], v25, s[10:11] offset:512
	global_load_dwordx4 v[56:59], v25, s[10:11] offset:640
	v_add_u32_dpp v42, v8, v8 row_shr:1 row_mask:0xf bank_mask:0xf bound_ctrl:1
	s_nop 1
	v_add_u32_dpp v42, v42, v42 row_shr:2 row_mask:0xf bank_mask:0xf bound_ctrl:1
	s_nop 1
	v_add_u32_dpp v42, v42, v42 row_shr:4 row_mask:0xf bank_mask:0xf bound_ctrl:1
	s_nop 1
	v_add_u32_dpp v42, v42, v42 row_shr:8 row_mask:0xf bank_mask:0xf bound_ctrl:1
	s_nop 1
	v_add_u32_dpp v42, v42, v42 row_bcast:15 row_mask:0xa bank_mask:0xf
	s_nop 1
	v_add_u32_dpp v42, v42, v42 row_bcast:31 row_mask:0xc bank_mask:0xf
	s_lshl_b32 s5, s4, 2
	v_mov_b32_e32 v43, s5
	v_readlane_b32 s5, v42, 63
	s_nop 3
	v_mov_b32_e32 v42, s5
	ds_write_b32 v43, v42 offset:19216
